# router phase (P10): x1 row loads use the default cache policy instead of non-temporal (each 128-B line is touched by 8 load instructions of a wave; keeps them in L1/L2 between the touches)
# speedup vs baseline: 1.0161x; 1.0088x over previous
.LBB0_1752:
	s_lshl_b32 s10, s41, 3
	s_add_i32 s30, s10, s97
	s_lshl_b32 s31, s30, 4
	v_or_b32_e32 v0, s31, v114
	v_ashrrev_i32_e32 v1, 31, v0
	v_lshlrev_b64 v[2:3], 7, v[0:1]
	v_lshl_add_u64 v[2:3], v[86:87], 0, v[2:3]
	global_load_dwordx4 v[104:107], v[2:3], off
	global_load_dwordx4 v[108:111], v[2:3], off offset:16
	s_ashr_i32 s10, s41, 4
	s_mul_hi_i32 s11, s10, 0xc000
	s_mul_i32 s10, s10, 0xc000
	s_add_u32 s10, s0, s10
	s_addc_u32 s11, s1, s11
	v_lshl_add_u64 v[2:3], v[90:91], 2, s[10:11]
	v_add_co_u32_e32 v4, vcc, s33, v2
	v_lshlrev_b64 v[0:1], 13, v[0:1]
	s_nop 0
	v_addc_co_u32_e32 v5, vcc, 0, v3, vcc
	global_load_dwordx4 v[126:129], v[4:5], off
	v_add_co_u32_e32 v2, vcc, s36, v2
	v_lshl_add_u64 v[100:101], v[84:85], 0, v[0:1]
	s_nop 0
	v_addc_co_u32_e32 v3, vcc, 0, v3, vcc
	global_load_dwordx4 v[130:133], v[2:3], off
	global_load_dwordx4 v[134:137], v[92:93], off
	global_load_dwordx4 v[138:141], v[82:83], off
	global_load_dwordx4 v[64:67], v[82:83], off offset:256
	global_load_dwordx4 v[48:51], v[100:101], off
	global_load_dwordx4 v[36:39], v[100:101], off offset:16
	global_load_dwordx4 v[16:19], v[100:101], off offset:32
	global_load_dwordx4 v[4:7], v[100:101], off offset:48
	global_load_dwordx4 v[56:59], v[100:101], off offset:256
	global_load_dwordx4 v[44:47], v[100:101], off offset:272
	global_load_dwordx4 v[24:27], v[100:101], off offset:288
	global_load_dwordx4 v[8:11], v[100:101], off offset:304
	global_load_dwordx4 v[12:15], v[100:101], off offset:560
	global_load_dwordx4 v[32:35], v[100:101], off offset:544
	global_load_dwordx4 v[52:55], v[100:101], off offset:528
	global_load_dwordx4 v[60:63], v[100:101], off offset:512
	global_load_dwordx4 v[0:3], v[100:101], off offset:816
	global_load_dwordx4 v[20:23], v[100:101], off offset:800
	global_load_dwordx4 v[28:31], v[100:101], off offset:784
	global_load_dwordx4 v[40:43], v[100:101], off offset:768
	v_ashrrev_i32_e32 v99, 31, v98
	v_mov_b64_e32 v[102:103], v[78:79]
	v_mov_b32_e32 v125, v115
	s_mov_b32 s12, s21
	v_mov_b32_e32 v68, 0
	v_mov_b32_e32 v69, v81
	v_mov_b32_e32 v70, v81
	v_mov_b32_e32 v71, v81
	v_mov_b32_e32 v72, 0
	v_mov_b32_e32 v73, v81
	v_mov_b32_e32 v74, v81
	s_waitcnt vmcnt(22)
	v_mov_b32_e32 v112, v104
	s_waitcnt vmcnt(21)
	v_mov_b32_e32 v113, v108
	v_mov_b32_e32 v108, v105
	v_mov_b32_e32 v104, v106
	v_mov_b32_e32 v105, v110
	v_mov_b32_e32 v110, v107
	v_pk_add_f32 v[106:107], v[112:113], v[108:109]
	v_pk_add_f32 v[104:105], v[104:105], v[110:111]
	s_waitcnt vmcnt(20)
	v_pk_add_f32 v[110:111], v[126:127], 1.0 op_sel_hi:[1,0]
	v_pk_add_f32 v[104:105], v[106:107], v[104:105]
	v_pk_add_f32 v[106:107], v[128:129], 1.0 op_sel_hi:[1,0]
	v_add_f32_e32 v75, v104, v105
	ds_bpermute_b32 v108, v116, v75
	v_lshlrev_b64 v[104:105], 11, v[98:99]
	v_lshl_add_u64 v[104:105], v[96:97], 0, v[104:105]
	s_waitcnt vmcnt(19)
	ds_write_b128 v118, v[130:133] offset:8192
	s_waitcnt lgkmcnt(1)
	v_add_f32_e32 v75, v75, v108
	ds_bpermute_b32 v99, v117, v75
	s_waitcnt vmcnt(18)
	v_pk_mul_f32 v[108:109], v[136:137], v[106:107]
	v_pk_mul_f32 v[106:107], v[134:135], v[110:111]
	ds_write_b128 v118, v[106:109]
	s_waitcnt vmcnt(17)
	ds_write_b128 v119, v[138:141] offset:16384
	s_waitcnt lgkmcnt(2)
	v_add_f32_e32 v75, v75, v99
	v_fmamk_f32 v75, v75, 0x3a000000, v120
	v_mul_f32_e32 v99, 0x4f800000, v75
	v_cmp_gt_f32_e32 vcc, s37, v75
	s_waitcnt lgkmcnt(0)
	s_barrier
	v_cndmask_b32_e32 v75, v75, v99, vcc
	v_sqrt_f32_e32 v99, v75
	s_nop 0
	v_add_u32_e32 v106, -1, v99
	v_add_u32_e32 v107, 1, v99
	v_fma_f32 v108, -v106, v99, v75
	v_fma_f32 v109, -v107, v99, v75
	v_cmp_ge_f32_e64 s[10:11], 0, v108
	s_nop 1
	v_cndmask_b32_e64 v99, v99, v106, s[10:11]
	v_cmp_lt_f32_e64 s[10:11], 0, v109
	s_nop 1
	v_cndmask_b32_e64 v99, v99, v107, s[10:11]
	v_mul_f32_e32 v106, 0x37800000, v99
	v_cndmask_b32_e32 v99, v99, v106, vcc
	v_cmp_class_f32_e32 vcc, v75, v121
	s_nop 1
	v_cndmask_b32_e32 v75, v99, v75, vcc
	v_div_scale_f32 v99, s[10:11], v75, v75, 1.0
	v_rcp_f32_e32 v106, v99
	v_div_scale_f32 v107, vcc, 1.0, v75, 1.0
	v_fma_f32 v108, -v99, v106, 1.0
	v_fmac_f32_e32 v106, v108, v106
	v_mul_f32_e32 v108, v107, v106
	v_fma_f32 v109, -v99, v108, v107
	v_fmac_f32_e32 v108, v109, v106
	v_fma_f32 v99, -v99, v108, v107
	v_div_fmas_f32 v99, v99, v106, v108
	v_div_fixup_f32 v106, v99, v75, 1.0
	v_mov_b32_e32 v107, v106
	v_mov_b32_e32 v108, v106
	v_mov_b32_e32 v109, v106
	v_mov_b32_e32 v75, v81
	s_branch .LBB0_1754
.LBB0_1753:
	ds_read_b128 v[126:129], v125 offset:8960
	ds_read_b128 v[130:133], v125 offset:768
	ds_read_b128 v[134:137], v125 offset:784
	ds_read_b128 v[138:141], v125 offset:8976
	v_pk_mul_f32 v[40:41], v[106:107], v[40:41]
	ds_read_b128 v[142:145], v123 offset:25088
	ds_read_b128 v[146:149], v123 offset:25104
	s_waitcnt lgkmcnt(4)
	v_pk_fma_f32 v[112:113], v[40:41], v[130:131], v[126:127]
	ds_read_b128 v[150:153], v123 offset:29440
	ds_read_b128 v[154:157], v123 offset:29456
	v_pk_mul_f32 v[40:41], v[108:109], v[42:43]
	v_pk_mul_f32 v[28:29], v[106:107], v[28:29]
	v_pk_mul_f32 v[20:21], v[106:107], v[20:21]
	s_waitcnt lgkmcnt(3)
	v_mfma_f32_16x16x4_f32 v[72:75], v112, v142, v[72:75]
	v_mul_f32_e64 v0, v106, v0
	v_mul_f32_e64 v1, v107, v1
	v_mul_f32_e64 v2, v108, v2
	v_mul_f32_e64 v3, v109, v3
	s_min_u32 s13, s12, 24
	s_lshl_b32 s20, s13, 8
	s_add_i32 s12, s12, 4
	v_lshl_add_u64 v[104:105], v[104:105], 0, s[22:23]
	v_lshl_add_u64 v[102:103], v[102:103], 0, s[28:29]
	s_waitcnt lgkmcnt(1)
	v_mfma_f32_16x16x4_f32 v[68:71], v112, v150, v[68:71]
	s_and_b64 vcc, exec, s[10:11]
	v_mfma_f32_16x16x4_f32 v[72:75], v113, v143, v[72:75]
	v_mfma_f32_16x16x4_f32 v[68:71], v113, v151, v[68:71]
	v_fma_f32 v150, v40, v132, v128
	v_fma_f32 v151, v41, v133, v129
	s_nop 0
	v_mfma_f32_16x16x4_f32 v[40:43], v150, v144, v[72:75]
	v_mfma_f32_16x16x4_f32 v[68:71], v150, v152, v[68:71]
	v_mfma_f32_16x16x4_f32 v[40:43], v151, v145, v[40:43]
	v_mfma_f32_16x16x4_f32 v[68:71], v151, v153, v[68:71]
	v_fma_f32 v152, v28, v134, v138
	v_fma_f32 v153, v29, v135, v139
	v_mul_f32_e64 v28, v108, v30
	v_mul_f32_e64 v29, v109, v31
	v_mfma_f32_16x16x4_f32 v[40:43], v152, v146, v[40:43]
	s_waitcnt lgkmcnt(0)
	v_mfma_f32_16x16x4_f32 v[68:71], v152, v154, v[68:71]
	v_mfma_f32_16x16x4_f32 v[40:43], v153, v147, v[40:43]
	v_mfma_f32_16x16x4_f32 v[68:71], v153, v155, v[68:71]
	v_fma_f32 v154, v28, v136, v140
	v_fma_f32 v155, v29, v137, v141
	s_nop 0
	v_mfma_f32_16x16x4_f32 v[28:31], v154, v148, v[40:43]
	v_mfma_f32_16x16x4_f32 v[40:43], v154, v156, v[68:71]
	s_nop 4
	ds_read_b128 v[68:71], v125 offset:8992
	ds_read_b128 v[72:75], v125 offset:800
	ds_read_b128 v[126:129], v125 offset:816
	ds_read_b128 v[130:133], v125 offset:9008
	ds_read_b128 v[134:137], v123 offset:25120
	ds_read_b128 v[138:141], v123 offset:25136
	v_add_u32_e32 v125, 0x400, v125
	s_waitcnt lgkmcnt(4)
	v_pk_fma_f32 v[68:69], v[20:21], v[72:73], v[68:69]
	v_pk_mul_f32 v[20:21], v[108:109], v[22:23]
	s_waitcnt lgkmcnt(2)
	v_pk_fma_f32 v[0:1], v[0:1], v[126:127], v[130:131]
	v_pk_fma_f32 v[70:71], v[20:21], v[74:75], v[70:71]
	v_mfma_f32_16x16x4_f32 v[28:31], v155, v149, v[28:31]
	ds_read_b128 v[142:145], v123 offset:29472
	ds_read_b128 v[146:149], v123 offset:29488
	v_mul_f32_e32 v72, 4.0, v154
	v_mul_f32_e32 v73, 4.0, v155
	v_mfma_f32_16x16x4_f32 v[40:43], v155, v157, v[40:43]
	s_waitcnt lgkmcnt(3)
	v_mfma_f32_16x16x4_f32 v[28:31], v68, v134, v[28:31]
	s_waitcnt lgkmcnt(1)
	v_mfma_f32_16x16x4_f32 v[40:43], v68, v142, v[40:43]
	v_mfma_f32_16x16x4_f32 v[28:31], v69, v135, v[28:31]
	v_mfma_f32_16x16x4_f32 v[40:43], v69, v143, v[40:43]
	v_mfma_f32_16x16x4_f32 v[20:23], v70, v136, v[28:31]
	v_mfma_f32_16x16x4_f32 v[28:31], v70, v144, v[40:43]
	s_nop 7
	v_mul_f32_e32 v41, 4.0, v112
	v_mul_f32_e32 v42, 4.0, v113
	v_mov_b32_e32 v40, 0
	v_cvt_pk_fp8_f32 v40, v41, v42
	v_mul_f32_e32 v41, 4.0, v150
	v_mul_f32_e32 v42, 4.0, v151
	v_mul_f32_e32 v43, 4.0, v153
	v_mfma_f32_16x16x4_f32 v[20:23], v71, v137, v[20:23]
	v_cvt_pk_fp8_f32 v40, v41, v42 op_sel:[0,0,1]
	v_mul_f32_e32 v42, 4.0, v152
	v_mov_b32_e32 v41, 0
	v_cvt_pk_fp8_f32 v41, v42, v43
	v_mul_f32_e32 v43, 4.0, v68
	v_mul_f32_e32 v68, 4.0, v69
	v_mov_b32_e32 v42, 0
	v_mfma_f32_16x16x4_f32 v[28:31], v71, v145, v[28:31]
	v_cvt_pk_fp8_f32 v42, v43, v68
	v_mul_f32_e32 v43, 4.0, v70
	v_mul_f32_e32 v68, 4.0, v71
	v_pk_fma_f32 v[112:113], v[2:3], v[128:129], v[132:133]
	v_cvt_pk_fp8_f32 v42, v43, v68 op_sel:[0,0,1]
	v_mov_b32_e32 v43, 0
	v_cvt_pk_fp8_f32 v41, v72, v73 op_sel:[0,0,1]
	v_mfma_f32_16x16x4_f32 v[20:23], v0, v138, v[20:23]
	s_waitcnt lgkmcnt(0)
	v_mfma_f32_16x16x4_f32 v[28:31], v0, v146, v[28:31]
	v_mul_f32_e32 v0, 4.0, v0
	v_mfma_f32_16x16x4_f32 v[20:23], v1, v139, v[20:23]
	v_mfma_f32_16x16x4_f32 v[28:31], v1, v147, v[28:31]
	v_mul_f32_e32 v1, 4.0, v1
	v_cvt_pk_fp8_f32 v43, v0, v1
	v_mul_f32_e32 v0, 4.0, v112
	v_mul_f32_e32 v1, 4.0, v113
	v_cvt_pk_fp8_f32 v43, v0, v1 op_sel:[0,0,1]
	global_store_dwordx4 v[110:111], v[40:43], off offset:192
	s_nop 1
	v_lshl_add_u64 v[40:41], v[100:101], 0, s[20:21]
	v_mfma_f32_16x16x4_f32 v[68:71], v112, v140, v[20:23]
	global_load_dwordx4 v[0:3], v[40:41], off offset:1840
	global_load_dwordx4 v[20:23], v[40:41], off offset:1824
	v_mfma_f32_16x16x4_f32 v[72:75], v112, v148, v[28:31]
	global_load_dwordx4 v[28:31], v[40:41], off offset:1808
	s_nop 0
	global_load_dwordx4 v[40:43], v[40:41], off offset:1792
	s_barrier
	v_mfma_f32_16x16x4_f32 v[68:71], v113, v141, v[68:71]
	v_mfma_f32_16x16x4_f32 v[72:75], v113, v149, v[72:75]
	s_cbranch_vccnz .LBB0_1756
.LBB0_1754:
	s_waitcnt vmcnt(5)
	ds_write_b128 v119, v[64:67] offset:25088
	ds_read_b128 v[64:67], v125
	ds_read_b128 v[110:113], v125 offset:8192
	s_waitcnt vmcnt(15)
	v_pk_mul_f32 v[48:49], v[106:107], v[48:49]
	ds_read_b128 v[126:129], v125 offset:16
	ds_read_b128 v[130:133], v125 offset:8208
	ds_read_b128 v[134:137], v123 offset:20736
	ds_read_b128 v[138:141], v123 offset:20752
	s_waitcnt vmcnt(14)
	v_pk_mul_f32 v[36:37], v[106:107], v[36:37]
	s_waitcnt lgkmcnt(4)
	v_pk_fma_f32 v[142:143], v[48:49], v[64:65], v[110:111]
	v_pk_mul_f32 v[48:49], v[108:109], v[50:51]
	s_waitcnt vmcnt(13)
	v_pk_mul_f32 v[16:17], v[106:107], v[16:17]
	s_waitcnt vmcnt(12)
	v_pk_mul_f32 v[4:5], v[106:107], v[4:5]
	s_min_u32 s10, s12, 27
	s_waitcnt lgkmcnt(1)
	v_mfma_f32_16x16x4_f32 v[72:75], v142, v134, v[72:75]
	s_lshl_b32 s20, s10, 8
	s_waitcnt vmcnt(11)
	v_mul_f32_e64 v56, v106, v56
	v_mul_f32_e64 v57, v107, v57
	s_waitcnt vmcnt(10)
	v_pk_mul_f32 v[44:45], v[106:107], v[44:45]
	s_waitcnt vmcnt(9)
	v_pk_mul_f32 v[24:25], v[106:107], v[24:25]
	s_waitcnt vmcnt(8)
	v_pk_mul_f32 v[8:9], v[106:107], v[8:9]
	s_min_u32 s10, s12, 26
	s_lshl_b32 s10, s10, 8
	v_mfma_f32_16x16x4_f32 v[72:75], v143, v135, v[72:75]
	v_fma_f32 v134, v48, v66, v112
	v_fma_f32 v135, v49, v67, v113
	s_mov_b32 s11, s21
	s_waitcnt vmcnt(4)
	v_mul_f32_e64 v60, v106, v60
	v_mul_f32_e64 v61, v107, v61
	v_pk_mul_f32 v[52:53], v[106:107], v[52:53]
	v_pk_mul_f32 v[32:33], v[106:107], v[32:33]
	v_pk_mul_f32 v[12:13], v[106:107], v[12:13]
	v_mfma_f32_16x16x4_f32 v[48:51], v134, v136, v[72:75]
	v_mfma_f32_16x16x4_f32 v[48:51], v135, v137, v[48:51]
	v_fma_f32 v136, v36, v126, v130
	v_fma_f32 v137, v37, v127, v131
	v_mul_f32_e64 v36, v108, v38
	v_mul_f32_e64 v37, v109, v39
	s_waitcnt lgkmcnt(0)
	v_mfma_f32_16x16x4_f32 v[48:51], v136, v138, v[48:51]
	v_mfma_f32_16x16x4_f32 v[48:51], v137, v139, v[48:51]
	v_fma_f32 v138, v36, v128, v132
	v_fma_f32 v139, v37, v129, v133
	s_nop 0
	v_mfma_f32_16x16x4_f32 v[36:39], v138, v140, v[48:51]
	s_nop 5
	ds_read_b128 v[48:51], v125 offset:32
	ds_read_b128 v[64:67], v125 offset:8224
	ds_read_b128 v[72:75], v125 offset:48
	ds_read_b128 v[110:113], v125 offset:8240
	ds_read_b128 v[126:129], v123 offset:20768
	ds_read_b128 v[130:133], v123 offset:20784
	s_waitcnt lgkmcnt(4)
	v_pk_fma_f32 v[48:49], v[16:17], v[48:49], v[64:65]
	v_pk_mul_f32 v[16:17], v[108:109], v[18:19]
	v_mfma_f32_16x16x4_f32 v[36:39], v139, v141, v[36:39]
	v_fma_f32 v50, v16, v50, v66
	v_fma_f32 v51, v17, v51, v67
	s_waitcnt lgkmcnt(1)
	v_mfma_f32_16x16x4_f32 v[36:39], v48, v126, v[36:39]
	v_mfma_f32_16x16x4_f32 v[36:39], v49, v127, v[36:39]
	v_fma_f32 v126, v4, v72, v110
	v_fma_f32 v127, v5, v73, v111
	v_mul_f32_e64 v4, v108, v6
	v_mul_f32_e64 v5, v109, v7
	v_fma_f32 v144, v4, v74, v112
	v_fma_f32 v145, v5, v75, v113
	v_lshl_add_u64 v[112:113], s[26:27], 0, v[102:103]
	v_add_co_u32_e32 v146, vcc, s38, v112
	v_mfma_f32_16x16x4_f32 v[16:19], v50, v128, v[36:39]
	s_nop 0
	v_addc_co_u32_e32 v147, vcc, 0, v113, vcc
	v_mfma_f32_16x16x4_f32 v[16:19], v51, v129, v[16:19]
	s_waitcnt lgkmcnt(0)
	v_mfma_f32_16x16x4_f32 v[16:19], v126, v130, v[16:19]
	v_mfma_f32_16x16x4_f32 v[16:19], v127, v131, v[16:19]
	v_mfma_f32_16x16x4_f32 v[4:7], v144, v132, v[16:19]
	v_mfma_f32_16x16x4_f32 v[64:67], v145, v133, v[4:7]
	s_nop 8
	ds_read_b128 v[4:7], v123 offset:16384
	ds_read_b128 v[16:19], v123 offset:16400
	global_load_dwordx4 v[72:75], v[146:147], off offset:512
	s_waitcnt lgkmcnt(1)
	v_mfma_f32_16x16x4_f32 v[36:39], v142, v4, v[68:71]
	ds_read_b128 v[68:71], v123 offset:16432
	v_mfma_f32_16x16x4_f32 v[36:39], v143, v5, v[36:39]
	v_mfma_f32_16x16x4_f32 v[36:39], v134, v6, v[36:39]
	v_mfma_f32_16x16x4_f32 v[4:7], v135, v7, v[36:39]
	s_nop 8
	v_mul_f32_e32 v36, 4.0, v142
	v_mul_f32_e32 v37, 4.0, v143
	s_waitcnt lgkmcnt(1)
	v_mfma_f32_16x16x4_f32 v[4:7], v136, v16, v[4:7]
	v_mfma_f32_16x16x4_f32 v[4:7], v137, v17, v[4:7]
	v_mfma_f32_16x16x4_f32 v[4:7], v138, v18, v[4:7]
	v_mfma_f32_16x16x4_f32 v[4:7], v139, v19, v[4:7]
	ds_read_b128 v[16:19], v123 offset:16416
	s_waitcnt lgkmcnt(0)
	v_mfma_f32_16x16x4_f32 v[4:7], v48, v16, v[4:7]
	v_mov_b32_e32 v16, 0
	v_cvt_pk_fp8_f32 v16, v36, v37
	v_mul_f32_e32 v36, 4.0, v134
	v_mul_f32_e32 v37, 4.0, v135
	v_cvt_pk_fp8_f32 v16, v36, v37 op_sel:[0,0,1]
	v_mul_f32_e32 v36, 4.0, v136
	v_mfma_f32_16x16x4_f32 v[4:7], v49, v17, v[4:7]
	v_mul_f32_e32 v37, 4.0, v137
	v_mov_b32_e32 v17, 0
	v_cvt_pk_fp8_f32 v17, v36, v37
	v_mul_f32_e32 v36, 4.0, v138
	v_mul_f32_e32 v37, 4.0, v139
	v_cvt_pk_fp8_f32 v17, v36, v37 op_sel:[0,0,1]
	v_mfma_f32_16x16x4_f32 v[4:7], v50, v18, v[4:7]
	v_mul_f32_e32 v36, 4.0, v48
	v_mul_f32_e32 v37, 4.0, v49
	v_mov_b32_e32 v18, 0
	v_cvt_pk_fp8_f32 v18, v36, v37
	v_mul_f32_e32 v36, 4.0, v50
	v_mul_f32_e32 v37, 4.0, v51
	v_lshl_add_u64 v[48:49], v[100:101], 0, s[20:21]
	v_mfma_f32_16x16x4_f32 v[4:7], v51, v19, v[4:7]
	v_cvt_pk_fp8_f32 v18, v36, v37 op_sel:[0,0,1]
	v_mul_f32_e32 v36, 4.0, v126
	v_mul_f32_e32 v37, 4.0, v127
	v_mov_b32_e32 v19, 0
	v_cvt_pk_fp8_f32 v19, v36, v37
	v_mul_f32_e32 v36, 4.0, v144
	v_mul_f32_e32 v37, 4.0, v145
	v_mfma_f32_16x16x4_f32 v[4:7], v126, v68, v[4:7]
	v_cvt_pk_fp8_f32 v19, v36, v37 op_sel:[0,0,1]
	v_lshl_add_u64 v[36:37], s[26:27], 0, v[104:105]
	v_add_co_u32_e32 v110, vcc, s39, v36
	s_nop 1
	v_addc_co_u32_e32 v111, vcc, 0, v37, vcc
	v_mfma_f32_16x16x4_f32 v[126:129], v127, v69, v[4:7]
	global_store_dwordx4 v[110:111], v[16:19], off
	s_nop 1
	global_load_dwordx4 v[4:7], v[48:49], off offset:1072
	global_load_dwordx4 v[16:19], v[48:49], off offset:1056
	global_load_dwordx4 v[36:39], v[48:49], off offset:1040
	s_nop 0
	global_load_dwordx4 v[48:51], v[48:49], off offset:1024
	s_barrier
	s_waitcnt vmcnt(5)
	ds_write_b128 v119, v[72:75] offset:16384
	ds_read_b128 v[72:75], v125 offset:8448
	ds_read_b128 v[130:133], v125 offset:256
	ds_read_b128 v[134:137], v125 offset:272
	ds_read_b128 v[138:141], v125 offset:8464
	v_mfma_f32_16x16x4_f32 v[126:129], v144, v70, v[126:129]
	s_waitcnt lgkmcnt(2)
	v_fma_f32 v148, v56, v130, v72
	v_fma_f32 v149, v57, v131, v73
	v_mul_f32_e64 v56, v108, v58
	v_mul_f32_e64 v57, v109, v59
	s_waitcnt lgkmcnt(0)
	v_pk_fma_f32 v[138:139], v[44:45], v[134:135], v[138:139]
	v_pk_fma_f32 v[150:151], v[56:57], v[132:133], v[74:75]
	v_pk_mul_f32 v[44:45], v[108:109], v[46:47]
	v_mfma_f32_16x16x4_f32 v[68:71], v145, v71, v[126:129]
	ds_read_b128 v[126:129], v123 offset:29440
	ds_read_b128 v[142:145], v123 offset:29456
	v_fma_f32 v140, v44, v136, v140
	v_fma_f32 v141, v45, v137, v141
	s_waitcnt lgkmcnt(1)
	v_mfma_f32_16x16x4_f32 v[64:67], v148, v126, v[64:67]
	v_mfma_f32_16x16x4_f32 v[64:67], v149, v127, v[64:67]
	v_mfma_f32_16x16x4_f32 v[56:59], v150, v128, v[64:67]
	v_mfma_f32_16x16x4_f32 v[56:59], v151, v129, v[56:59]
	s_waitcnt lgkmcnt(0)
	v_mfma_f32_16x16x4_f32 v[56:59], v138, v142, v[56:59]
	v_mfma_f32_16x16x4_f32 v[56:59], v139, v143, v[56:59]
	v_mfma_f32_16x16x4_f32 v[44:47], v140, v144, v[56:59]
	s_nop 8
	ds_read_b128 v[56:59], v125 offset:8480
	ds_read_b128 v[64:67], v125 offset:288
	ds_read_b128 v[72:75], v125 offset:304
	ds_read_b128 v[126:129], v125 offset:8496
	ds_read_b128 v[130:133], v123 offset:29472
	ds_read_b128 v[134:137], v123 offset:29488
	s_waitcnt lgkmcnt(4)
	v_pk_fma_f32 v[56:57], v[24:25], v[64:65], v[56:57]
	v_pk_mul_f32 v[24:25], v[108:109], v[26:27]
	s_waitcnt lgkmcnt(2)
	v_pk_fma_f32 v[126:127], v[8:9], v[72:73], v[126:127]
	v_pk_fma_f32 v[58:59], v[24:25], v[66:67], v[58:59]
	v_mfma_f32_16x16x4_f32 v[44:47], v141, v145, v[44:47]
	v_mul_f32_e64 v8, v108, v10
	v_mul_f32_e64 v9, v109, v11
	s_waitcnt lgkmcnt(1)
	v_mfma_f32_16x16x4_f32 v[44:47], v56, v130, v[44:47]
	v_mfma_f32_16x16x4_f32 v[44:47], v57, v131, v[44:47]
	v_mfma_f32_16x16x4_f32 v[24:27], v58, v132, v[44:47]
	v_mfma_f32_16x16x4_f32 v[24:27], v59, v133, v[24:27]
	s_waitcnt lgkmcnt(0)
	v_mfma_f32_16x16x4_f32 v[24:27], v126, v134, v[24:27]
	v_mfma_f32_16x16x4_f32 v[24:27], v127, v135, v[24:27]
	v_fma_f32 v134, v8, v74, v128
	v_fma_f32 v135, v9, v75, v129
	s_nop 0
	v_mfma_f32_16x16x4_f32 v[8:11], v134, v136, v[24:27]
	v_mfma_f32_16x16x4_f32 v[64:67], v135, v137, v[8:11]
	s_nop 8
	ds_read_b128 v[8:11], v123 offset:25088
	ds_read_b128 v[24:27], v123 offset:25104
	s_waitcnt lgkmcnt(1)
	v_mfma_f32_16x16x4_f32 v[44:47], v148, v8, v[68:71]
	v_mfma_f32_16x16x4_f32 v[44:47], v149, v9, v[44:47]
	v_mfma_f32_16x16x4_f32 v[44:47], v150, v10, v[44:47]
	v_mfma_f32_16x16x4_f32 v[8:11], v151, v11, v[44:47]
	s_nop 8
	v_mul_f32_e32 v44, 4.0, v148
	v_mul_f32_e32 v45, 4.0, v149
	v_mul_f32_e32 v46, 4.0, v150
	v_mul_f32_e32 v47, 4.0, v151
	s_waitcnt lgkmcnt(0)
	v_mfma_f32_16x16x4_f32 v[8:11], v138, v24, v[8:11]
	v_mfma_f32_16x16x4_f32 v[8:11], v139, v25, v[8:11]
	v_mfma_f32_16x16x4_f32 v[8:11], v140, v26, v[8:11]
	v_mfma_f32_16x16x4_f32 v[8:11], v141, v27, v[8:11]
	ds_read_b128 v[24:27], v123 offset:25120
	ds_read_b128 v[68:71], v123 offset:25136
	global_load_dwordx4 v[72:75], v[146:147], off offset:768
	s_waitcnt lgkmcnt(1)
	v_mfma_f32_16x16x4_f32 v[8:11], v56, v24, v[8:11]
	v_mov_b32_e32 v24, 0
	v_cvt_pk_fp8_f32 v24, v44, v45
	v_mul_f32_e32 v44, 4.0, v138
	v_mul_f32_e32 v45, 4.0, v139
	v_cvt_pk_fp8_f32 v24, v46, v47 op_sel:[0,0,1]
	v_mul_f32_e32 v46, 4.0, v58
	v_mfma_f32_16x16x4_f32 v[8:11], v57, v25, v[8:11]
	v_mov_b32_e32 v25, 0
	v_cvt_pk_fp8_f32 v25, v44, v45
	v_mul_f32_e32 v44, 4.0, v141
	v_mul_f32_e32 v45, 4.0, v57
	v_mul_f32_e32 v47, 4.0, v59
	v_mfma_f32_16x16x4_f32 v[8:11], v58, v26, v[8:11]
	v_mul_f32_e32 v26, 4.0, v140
	v_cvt_pk_fp8_f32 v25, v26, v44 op_sel:[0,0,1]
	v_mul_f32_e32 v44, 4.0, v56
	v_mov_b32_e32 v26, 0
	v_cvt_pk_fp8_f32 v26, v44, v45
	v_mul_f32_e32 v44, 4.0, v126
	v_mul_f32_e32 v45, 4.0, v127
	v_mfma_f32_16x16x4_f32 v[8:11], v59, v27, v[8:11]
	v_mov_b32_e32 v27, 0
	v_cvt_pk_fp8_f32 v27, v44, v45
	v_mul_f32_e32 v44, 4.0, v134
	v_mul_f32_e32 v45, 4.0, v135
	v_cvt_pk_fp8_f32 v26, v46, v47 op_sel:[0,0,1]
	v_cvt_pk_fp8_f32 v27, v44, v45 op_sel:[0,0,1]
	v_lshl_add_u64 v[56:57], v[100:101], 0, s[10:11]
	s_waitcnt lgkmcnt(0)
	v_mfma_f32_16x16x4_f32 v[8:11], v126, v68, v[8:11]
	s_min_u32 s10, s12, 25
	global_store_dwordx4 v[110:111], v[24:27], off offset:64
	v_mfma_f32_16x16x4_f32 v[44:47], v127, v69, v[8:11]
	s_nop 6
	global_load_dwordx4 v[8:11], v[56:57], off offset:1328
	global_load_dwordx4 v[24:27], v[56:57], off offset:1312
	v_mfma_f32_16x16x4_f32 v[126:129], v134, v70, v[44:47]
	global_load_dwordx4 v[44:47], v[56:57], off offset:1296
	s_nop 0
	global_load_dwordx4 v[56:59], v[56:57], off offset:1280
	s_barrier
	s_waitcnt vmcnt(5)
	ds_write_b128 v119, v[72:75] offset:25088
	ds_read_b128 v[72:75], v125 offset:512
	ds_read_b128 v[130:133], v125 offset:8704
	v_mfma_f32_16x16x4_f32 v[126:129], v135, v71, v[126:129]
	ds_read_b128 v[68:71], v125 offset:528
	ds_read_b128 v[134:137], v125 offset:8720
	ds_read_b128 v[138:141], v123 offset:20736
	ds_read_b128 v[142:145], v123 offset:20752
	s_waitcnt lgkmcnt(4)
	v_pk_fma_f32 v[146:147], v[60:61], v[72:73], v[130:131]
	v_pk_mul_f32 v[60:61], v[108:109], v[62:63]
	s_waitcnt lgkmcnt(1)
	v_mfma_f32_16x16x4_f32 v[64:67], v146, v138, v[64:67]
	v_mfma_f32_16x16x4_f32 v[64:67], v147, v139, v[64:67]
	v_fma_f32 v138, v60, v74, v132
	v_fma_f32 v139, v61, v75, v133
	s_nop 0
	v_mfma_f32_16x16x4_f32 v[60:63], v138, v140, v[64:67]
	v_mfma_f32_16x16x4_f32 v[60:63], v139, v141, v[60:63]
	v_fma_f32 v140, v52, v68, v134
	v_fma_f32 v141, v53, v69, v135
	v_mul_f32_e64 v52, v108, v54
	v_mul_f32_e64 v53, v109, v55
	s_waitcnt lgkmcnt(0)
	v_mfma_f32_16x16x4_f32 v[60:63], v140, v142, v[60:63]
	v_mfma_f32_16x16x4_f32 v[60:63], v141, v143, v[60:63]
	v_fma_f32 v142, v52, v70, v136
	v_fma_f32 v143, v53, v71, v137
	s_nop 0
	v_mfma_f32_16x16x4_f32 v[52:55], v142, v144, v[60:63]
	s_nop 5
	ds_read_b128 v[60:63], v125 offset:8736
	ds_read_b128 v[64:67], v125 offset:544
	ds_read_b128 v[68:71], v125 offset:560
	ds_read_b128 v[72:75], v125 offset:8752
	ds_read_b128 v[130:133], v123 offset:20768
	ds_read_b128 v[134:137], v123 offset:20784
	s_waitcnt lgkmcnt(4)
	v_pk_fma_f32 v[60:61], v[32:33], v[64:65], v[60:61]
	v_pk_mul_f32 v[32:33], v[108:109], v[34:35]
	s_waitcnt lgkmcnt(2)
	v_pk_fma_f32 v[64:65], v[12:13], v[68:69], v[72:73]
	v_pk_fma_f32 v[62:63], v[32:33], v[66:67], v[62:63]
	v_mfma_f32_16x16x4_f32 v[52:55], v143, v145, v[52:55]
	v_mul_f32_e64 v12, v108, v14
	v_mul_f32_e64 v13, v109, v15
	s_waitcnt lgkmcnt(1)
	v_mfma_f32_16x16x4_f32 v[52:55], v60, v130, v[52:55]
	v_mfma_f32_16x16x4_f32 v[52:55], v61, v131, v[52:55]
	v_fma_f32 v130, v12, v70, v74
	v_fma_f32 v131, v13, v71, v75
	v_mfma_f32_16x16x4_f32 v[32:35], v62, v132, v[52:55]
	v_mfma_f32_16x16x4_f32 v[32:35], v63, v133, v[32:35]
	s_waitcnt lgkmcnt(0)
	v_mfma_f32_16x16x4_f32 v[32:35], v64, v134, v[32:35]
	v_mfma_f32_16x16x4_f32 v[32:35], v65, v135, v[32:35]
	v_mfma_f32_16x16x4_f32 v[12:15], v130, v136, v[32:35]
	v_mfma_f32_16x16x4_f32 v[68:71], v131, v137, v[12:15]
	s_nop 8
	ds_read_b128 v[12:15], v123 offset:16384
	ds_read_b128 v[32:35], v123 offset:16400
	s_waitcnt lgkmcnt(1)
	v_mfma_f32_16x16x4_f32 v[52:55], v146, v12, v[126:129]
	v_mfma_f32_16x16x4_f32 v[52:55], v147, v13, v[52:55]
	v_mfma_f32_16x16x4_f32 v[52:55], v138, v14, v[52:55]
	v_mfma_f32_16x16x4_f32 v[12:15], v139, v15, v[52:55]
	s_nop 8
	v_mul_f32_e32 v52, 4.0, v146
	v_mul_f32_e32 v55, 4.0, v141
	v_mul_f32_e32 v53, 4.0, v138
	v_mul_f32_e32 v54, 4.0, v139
	s_waitcnt lgkmcnt(0)
	v_mfma_f32_16x16x4_f32 v[12:15], v140, v32, v[12:15]
	v_mfma_f32_16x16x4_f32 v[12:15], v141, v33, v[12:15]
	v_mfma_f32_16x16x4_f32 v[12:15], v142, v34, v[12:15]
	v_mfma_f32_16x16x4_f32 v[12:15], v143, v35, v[12:15]
	ds_read_b128 v[32:35], v123 offset:16416
	ds_read_b128 v[72:75], v123 offset:16432
	s_waitcnt lgkmcnt(1)
	v_mfma_f32_16x16x4_f32 v[12:15], v60, v32, v[12:15]
	v_mov_b32_e32 v32, 0
	v_mfma_f32_16x16x4_f32 v[12:15], v61, v33, v[12:15]
	v_mul_f32_e32 v33, 4.0, v147
	v_cvt_pk_fp8_f32 v32, v52, v33
	v_mul_f32_e32 v52, 4.0, v140
	v_mov_b32_e32 v33, 0
	v_cvt_pk_fp8_f32 v33, v52, v55
	v_mul_f32_e32 v52, 4.0, v143
	v_mul_f32_e32 v55, 4.0, v65
	v_mfma_f32_16x16x4_f32 v[12:15], v62, v34, v[12:15]
	v_mul_f32_e32 v34, 4.0, v142
	v_cvt_pk_fp8_f32 v33, v34, v52 op_sel:[0,0,1]
	v_mul_f32_e32 v52, 4.0, v60
	v_mov_b32_e32 v34, 0
	v_cvt_pk_fp8_f32 v32, v53, v54 op_sel:[0,0,1]
	v_mul_f32_e32 v53, 4.0, v62
	v_mul_f32_e32 v54, 4.0, v63
	v_mfma_f32_16x16x4_f32 v[12:15], v63, v35, v[12:15]
	v_mul_f32_e32 v35, 4.0, v61
	v_cvt_pk_fp8_f32 v34, v52, v35
	v_mul_f32_e32 v52, 4.0, v64
	v_mov_b32_e32 v35, 0
	v_cvt_pk_fp8_f32 v35, v52, v55
	v_cvt_pk_fp8_f32 v34, v53, v54 op_sel:[0,0,1]
	v_mul_f32_e32 v52, 4.0, v130
	s_waitcnt lgkmcnt(0)
	v_mfma_f32_16x16x4_f32 v[12:15], v64, v72, v[12:15]
	v_mul_f32_e32 v53, 4.0, v131
	v_cvt_pk_fp8_f32 v35, v52, v53 op_sel:[0,0,1]
	v_lshl_add_u64 v[60:61], v[82:83], 0, s[20:21]
	s_lshl_b32 s20, s10, 8
	s_cmp_gt_u32 s12, 27
	s_cselect_b64 s[10:11], -1, 0
	s_and_b64 vcc, exec, s[10:11]
	v_mfma_f32_16x16x4_f32 v[52:55], v65, v73, v[12:15]
	global_load_dwordx4 v[64:67], v[60:61], off offset:1024
	v_lshl_add_u64 v[60:61], v[100:101], 0, s[20:21]
	global_store_dwordx4 v[110:111], v[32:35], off offset:128
	global_load_dwordx4 v[12:15], v[60:61], off offset:1584
	s_nop 0
	global_load_dwordx4 v[32:35], v[60:61], off offset:1568
	v_mfma_f32_16x16x4_f32 v[126:129], v130, v74, v[52:55]
	s_nop 2
	global_load_dwordx4 v[52:55], v[60:61], off offset:1552
	s_nop 0
	global_load_dwordx4 v[60:63], v[60:61], off offset:1536
	s_barrier
	v_mfma_f32_16x16x4_f32 v[72:75], v131, v75, v[126:129]
	s_cbranch_vccnz .LBB0_1753
	s_waitcnt vmcnt(5)
	ds_write_b128 v119, v[64:67] offset:16384
	v_add_co_u32_e32 v64, vcc, 0x910000, v112
	s_nop 1
	v_addc_co_u32_e32 v65, vcc, 0, v113, vcc
	global_load_dwordx4 v[64:67], v[64:65], off offset:1280
	s_branch .LBB0_1753
